# v24 plus sc1 nt cache policy on the A stream loads
# speedup vs baseline: 1.0192x; 1.0036x over previous
.LBB1_248:
	v_and_b32_e32 v6, 31, v0
	v_bfe_u32 v7, v0, 5, 3
	s_cmp_lt_u32 s8, 0x2000
	s_cselect_b32 s50, s12, s14
	s_cselect_b32 s51, s13, s15
	s_and_b32 s0, s8, 0x1fff
	s_mul_i32 s1, s0, 0x2ee0
	s_add_u32 s50, s50, s1
	s_addc_u32 s51, s51, 0
	s_mov_b32 s52, s50
	s_mov_b32 s53, s51
	s_add_u32 s54, s50, 0x17700
	s_addc_u32 s55, s51, 0
	s_add_u32 s56, s50, 0x2ee00
	s_addc_u32 s57, s51, 0
	s_add_u32 s58, s50, 0x46500
	s_addc_u32 s59, s51, 0
	s_add_u32 s60, s50, 0x5dc00
	s_addc_u32 s61, s51, 0
	s_add_u32 s62, s50, 0x75300
	s_addc_u32 s63, s51, 0
	s_add_u32 s64, s50, 0x8ca00
	s_addc_u32 s65, s51, 0
	s_add_u32 s66, s50, 0xa4100
	s_addc_u32 s67, s51, 0
	v_and_b32_e32 v104, 3, v7
	v_lshl_add_u32 v106, v104, 1, v6
	s_movk_i32 s0, 0x2ee0
	v_mul_lo_u32 v2, v7, s0
	v_lshl_add_u32 v2, v106, 4, v2
	s_movk_i32 s0, 0x110
	v_mul_lo_u32 v3, v7, s0
	v_lshl_add_u32 v107, v106, 3, v3
	v_cmp_le_u32_e64 s[76:77], 32, v106
	v_cmp_gt_u32_e64 s[68:69], 14, v106
	s_not_b64 s[78:79], s[76:77]
	v_mov_b32_e32 v108, 0x0
	v_mov_b32_e32 v109, 0x4300
	v_cndmask_b32_e64 v108, v108, v109, s[76:77]
	v_add_u32_e32 v110, v107, v108
	v_mov_b32_e32 v108, 0x4400
	v_mov_b32_e32 v109, 0x8700
	v_cndmask_b32_e64 v108, v108, v109, s[76:77]
	v_add_u32_e32 v111, v107, v108
	v_mov_b32_e32 v108, 0x8800
	v_mov_b32_e32 v109, 0xffffff00
	v_cndmask_b32_e64 v108, v108, v109, s[76:77]
	v_add_u32_e32 v112, v107, v108
	s_add_u32 s48, s18, 0x100000
	s_addc_u32 s49, s19, 0
	s_lshl_b32 s0, s10, 12
	v_add_u32_e32 v150, 0xfffffe00, v0
	v_lshl_add_u32 v150, v150, 4, s0
	global_load_dwordx4 v[152:155], v150, s[48:49]
	global_load_dwordx4 v[156:159], v150, s[18:19]
	v_mov_b32_e32 v116, 0
	v_mov_b32_e32 v117, 0
	v_mov_b32_e32 v118, 0
	v_mov_b32_e32 v119, 0
	s_mov_b64 s[70:71], exec
	s_mov_b64 exec, s[76:77]
	global_load_dwordx4 v[116:119], v2, s[52:53] offset:-512 sc1 nt
	s_mov_b64 exec, s[70:71]
	v_mov_b32_e32 v120, 0
	v_mov_b32_e32 v121, 0
	v_mov_b32_e32 v122, 0
	v_mov_b32_e32 v123, 0
	s_mov_b64 s[70:71], exec
	s_mov_b64 exec, s[76:77]
	global_load_dwordx4 v[120:123], v2, s[54:55] offset:-512 sc1 nt
	s_mov_b64 exec, s[70:71]
	v_mov_b32_e32 v124, 0
	v_mov_b32_e32 v125, 0
	v_mov_b32_e32 v126, 0
	v_mov_b32_e32 v127, 0
	s_mov_b64 s[70:71], exec
	s_mov_b64 exec, s[76:77]
	global_load_dwordx4 v[124:127], v2, s[56:57] offset:-512 sc1 nt
	s_mov_b64 exec, s[70:71]
	v_mov_b32_e32 v128, 0
	v_mov_b32_e32 v129, 0
	v_mov_b32_e32 v130, 0
	v_mov_b32_e32 v131, 0
	s_mov_b64 s[70:71], exec
	s_mov_b64 exec, s[76:77]
	global_load_dwordx4 v[128:131], v2, s[58:59] offset:-512 sc1 nt
	s_mov_b64 exec, s[70:71]
	v_mov_b32_e32 v132, 0
	v_mov_b32_e32 v133, 0
	v_mov_b32_e32 v134, 0
	v_mov_b32_e32 v135, 0
	s_mov_b64 s[70:71], exec
	s_mov_b64 exec, s[76:77]
	global_load_dwordx4 v[132:135], v2, s[60:61] offset:-512 sc1 nt
	s_mov_b64 exec, s[70:71]
	v_mov_b32_e32 v136, 0
	v_mov_b32_e32 v137, 0
	v_mov_b32_e32 v138, 0
	v_mov_b32_e32 v139, 0
	s_mov_b64 s[70:71], exec
	s_mov_b64 exec, s[76:77]
	global_load_dwordx4 v[136:139], v2, s[62:63] offset:-512 sc1 nt
	s_mov_b64 exec, s[70:71]
	v_mov_b32_e32 v140, 0
	v_mov_b32_e32 v141, 0
	v_mov_b32_e32 v142, 0
	v_mov_b32_e32 v143, 0
	s_mov_b64 s[70:71], exec
	s_mov_b64 exec, s[76:77]
	global_load_dwordx4 v[140:143], v2, s[64:65] offset:-512 sc1 nt
	s_mov_b64 exec, s[70:71]
	v_mov_b32_e32 v144, 0
	v_mov_b32_e32 v145, 0
	v_mov_b32_e32 v146, 0
	v_mov_b32_e32 v147, 0
	s_mov_b64 s[70:71], exec
	s_mov_b64 exec, s[76:77]
	global_load_dwordx4 v[144:147], v2, s[66:67] offset:-512 sc1 nt
	s_mov_b64 exec, s[70:71]
	global_load_dwordx4 v[8:11], v2, s[52:53] sc1 nt
	global_load_dwordx4 v[12:15], v2, s[54:55] sc1 nt
	global_load_dwordx4 v[16:19], v2, s[56:57] sc1 nt
	global_load_dwordx4 v[20:23], v2, s[58:59] sc1 nt
	global_load_dwordx4 v[24:27], v2, s[60:61] sc1 nt
	global_load_dwordx4 v[28:31], v2, s[62:63] sc1 nt
	global_load_dwordx4 v[32:35], v2, s[64:65] sc1 nt
	global_load_dwordx4 v[36:39], v2, s[66:67] sc1 nt
	global_load_dwordx4 v[40:43], v2, s[52:53] offset:512 sc1 nt
	global_load_dwordx4 v[44:47], v2, s[54:55] offset:512 sc1 nt
	global_load_dwordx4 v[48:51], v2, s[56:57] offset:512 sc1 nt
	global_load_dwordx4 v[52:55], v2, s[58:59] offset:512 sc1 nt
	global_load_dwordx4 v[56:59], v2, s[60:61] offset:512 sc1 nt
	global_load_dwordx4 v[60:63], v2, s[62:63] offset:512 sc1 nt
	global_load_dwordx4 v[64:67], v2, s[64:65] offset:512 sc1 nt
	global_load_dwordx4 v[68:71], v2, s[66:67] offset:512 sc1 nt
	global_load_dwordx4 v[72:75], v2, s[52:53] offset:1024 sc1 nt
	global_load_dwordx4 v[76:79], v2, s[54:55] offset:1024 sc1 nt
	global_load_dwordx4 v[80:83], v2, s[56:57] offset:1024 sc1 nt
	global_load_dwordx4 v[84:87], v2, s[58:59] offset:1024 sc1 nt
	global_load_dwordx4 v[88:91], v2, s[60:61] offset:1024 sc1 nt
	global_load_dwordx4 v[92:95], v2, s[62:63] offset:1024 sc1 nt
	global_load_dwordx4 v[96:99], v2, s[64:65] offset:1024 sc1 nt
	global_load_dwordx4 v[100:103], v2, s[66:67] offset:1024 sc1 nt
	s_waitcnt vmcnt(32)
	v_mov_b32_e32 v151, 1
	v_lshlrev_b32_e32 v160, 2, v152
	v_lshlrev_b32_e32 v161, 2, v153
	v_lshlrev_b32_e32 v162, 2, v154
	v_lshlrev_b32_e32 v163, 2, v155
	global_atomic_add v164, v160, v151, s[20:21] sc0
	global_atomic_add v165, v161, v151, s[20:21] sc0
	global_atomic_add v166, v162, v151, s[20:21] sc0
	global_atomic_add v167, v163, v151, s[20:21] sc0
	s_waitcnt vmcnt(35)
	v_cvt_pk_f16_f32 v4, v116, v117
	v_cvt_pk_f16_f32 v5, v118, v119
	s_mov_b64 s[70:71], exec
	s_mov_b64 exec, s[76:77]
	ds_write_b64 v112, v[4:5]
	s_mov_b64 exec, s[70:71]
	s_waitcnt vmcnt(34)
	v_cvt_pk_f16_f32 v4, v120, v121
	v_cvt_pk_f16_f32 v5, v122, v123
	s_mov_b64 s[70:71], exec
	s_mov_b64 exec, s[76:77]
	ds_write_b64 v112, v[4:5] offset:2176
	s_mov_b64 exec, s[70:71]
	s_waitcnt vmcnt(33)
	v_cvt_pk_f16_f32 v4, v124, v125
	v_cvt_pk_f16_f32 v5, v126, v127
	s_mov_b64 s[70:71], exec
	s_mov_b64 exec, s[76:77]
	ds_write_b64 v112, v[4:5] offset:4352
	s_mov_b64 exec, s[70:71]
	s_waitcnt vmcnt(32)
	v_cvt_pk_f16_f32 v4, v128, v129
	v_cvt_pk_f16_f32 v5, v130, v131
	s_mov_b64 s[70:71], exec
	s_mov_b64 exec, s[76:77]
	ds_write_b64 v112, v[4:5] offset:6528
	s_mov_b64 exec, s[70:71]
	s_waitcnt vmcnt(31)
	v_cvt_pk_f16_f32 v4, v132, v133
	v_cvt_pk_f16_f32 v5, v134, v135
	s_mov_b64 s[70:71], exec
	s_mov_b64 exec, s[76:77]
	ds_write_b64 v112, v[4:5] offset:8704
	s_mov_b64 exec, s[70:71]
	s_waitcnt vmcnt(30)
	v_cvt_pk_f16_f32 v4, v136, v137
	v_cvt_pk_f16_f32 v5, v138, v139
	s_mov_b64 s[70:71], exec
	s_mov_b64 exec, s[76:77]
	ds_write_b64 v112, v[4:5] offset:10880
	s_mov_b64 exec, s[70:71]
	s_waitcnt vmcnt(29)
	v_cvt_pk_f16_f32 v4, v140, v141
	v_cvt_pk_f16_f32 v5, v142, v143
	s_mov_b64 s[70:71], exec
	s_mov_b64 exec, s[76:77]
	ds_write_b64 v112, v[4:5] offset:13056
	s_mov_b64 exec, s[70:71]
	s_waitcnt vmcnt(28)
	v_cvt_pk_f16_f32 v4, v144, v145
	v_cvt_pk_f16_f32 v5, v146, v147
	s_mov_b64 s[70:71], exec
	s_mov_b64 exec, s[76:77]
	ds_write_b64 v112, v[4:5] offset:15232
	s_mov_b64 exec, s[70:71]
	s_waitcnt vmcnt(27)
	v_cvt_pk_f16_f32 v4, v8, v9
	v_cvt_pk_f16_f32 v5, v10, v11
	ds_write_b64 v110, v[4:5]
	global_load_dwordx4 v[8:11], v2, s[52:53] offset:1536 sc1 nt
	s_waitcnt vmcnt(27)
	v_cvt_pk_f16_f32 v4, v12, v13
	v_cvt_pk_f16_f32 v5, v14, v15
	ds_write_b64 v110, v[4:5] offset:2176
	global_load_dwordx4 v[12:15], v2, s[54:55] offset:1536 sc1 nt
	s_waitcnt vmcnt(27)
	v_cvt_pk_f16_f32 v4, v16, v17
	v_cvt_pk_f16_f32 v5, v18, v19
	ds_write_b64 v110, v[4:5] offset:4352
	global_load_dwordx4 v[16:19], v2, s[56:57] offset:1536 sc1 nt
	s_waitcnt vmcnt(27)
	v_cvt_pk_f16_f32 v4, v20, v21
	v_cvt_pk_f16_f32 v5, v22, v23
	ds_write_b64 v110, v[4:5] offset:6528
	global_load_dwordx4 v[20:23], v2, s[58:59] offset:1536 sc1 nt
	s_waitcnt vmcnt(27)
	v_cvt_pk_f16_f32 v4, v24, v25
	v_cvt_pk_f16_f32 v5, v26, v27
	ds_write_b64 v110, v[4:5] offset:8704
	global_load_dwordx4 v[24:27], v2, s[60:61] offset:1536 sc1 nt
	s_waitcnt vmcnt(27)
	v_cvt_pk_f16_f32 v4, v28, v29
	v_cvt_pk_f16_f32 v5, v30, v31
	ds_write_b64 v110, v[4:5] offset:10880
	global_load_dwordx4 v[28:31], v2, s[62:63] offset:1536 sc1 nt
	s_waitcnt vmcnt(27)
	v_cvt_pk_f16_f32 v4, v32, v33
	v_cvt_pk_f16_f32 v5, v34, v35
	ds_write_b64 v110, v[4:5] offset:13056
	global_load_dwordx4 v[32:35], v2, s[64:65] offset:1536 sc1 nt
	s_waitcnt vmcnt(27)
	v_cvt_pk_f16_f32 v4, v36, v37
	v_cvt_pk_f16_f32 v5, v38, v39
	ds_write_b64 v110, v[4:5] offset:15232
	global_load_dwordx4 v[36:39], v2, s[66:67] offset:1536 sc1 nt
	s_waitcnt vmcnt(0)
	v_cmp_gt_i32_e32 vcc, 64, v164
	v_lshl_add_u32 v148, v152, 6, v164
	v_lshlrev_b32_e32 v148, 2, v148
	s_and_saveexec_b64 s[2:3], vcc
	global_store_dword v148, v156, s[22:23]
	s_xor_b64 exec, exec, s[2:3]
	s_cbranch_execz .Lg1_ld_ok_0
	v_mov_b32_e32 v149, 0x8000
	global_atomic_add v149, v149, v151, s[20:21] sc0
	s_waitcnt vmcnt(0)
	v_lshlrev_b32_e32 v149, 3, v149
	v_mov_b32_e32 v160, v152
	v_mov_b32_e32 v161, v156
	global_store_dwordx2 v149, v[160:161], s[28:29]

.Lg1_ld_ok_3:
	s_mov_b64 exec, -1
	s_waitcnt lgkmcnt(0)
	s_barrier
	s_waitcnt vmcnt(27)
	v_cvt_pk_f16_f32 v4, v40, v41
	v_cvt_pk_f16_f32 v5, v42, v43
	ds_write_b64 v111, v[4:5]
	global_load_dwordx4 v[40:43], v2, s[52:53] offset:2048 sc1 nt
	s_waitcnt vmcnt(27)
	v_cvt_pk_f16_f32 v4, v44, v45
	v_cvt_pk_f16_f32 v5, v46, v47
	ds_write_b64 v111, v[4:5] offset:2176
	global_load_dwordx4 v[44:47], v2, s[54:55] offset:2048 sc1 nt
	s_waitcnt vmcnt(27)
	v_cvt_pk_f16_f32 v4, v48, v49
	v_cvt_pk_f16_f32 v5, v50, v51
	ds_write_b64 v111, v[4:5] offset:4352
	global_load_dwordx4 v[48:51], v2, s[56:57] offset:2048 sc1 nt
	s_waitcnt vmcnt(27)
	v_cvt_pk_f16_f32 v4, v52, v53
	v_cvt_pk_f16_f32 v5, v54, v55
	ds_write_b64 v111, v[4:5] offset:6528
	global_load_dwordx4 v[52:55], v2, s[58:59] offset:2048 sc1 nt
	s_waitcnt vmcnt(27)
	v_cvt_pk_f16_f32 v4, v56, v57
	v_cvt_pk_f16_f32 v5, v58, v59
	ds_write_b64 v111, v[4:5] offset:8704
	global_load_dwordx4 v[56:59], v2, s[60:61] offset:2048 sc1 nt
	s_waitcnt vmcnt(27)
	v_cvt_pk_f16_f32 v4, v60, v61
	v_cvt_pk_f16_f32 v5, v62, v63
	ds_write_b64 v111, v[4:5] offset:10880
	global_load_dwordx4 v[60:63], v2, s[62:63] offset:2048 sc1 nt
	s_waitcnt vmcnt(27)
	v_cvt_pk_f16_f32 v4, v64, v65
	v_cvt_pk_f16_f32 v5, v66, v67
	ds_write_b64 v111, v[4:5] offset:13056
	global_load_dwordx4 v[64:67], v2, s[64:65] offset:2048 sc1 nt
	s_waitcnt vmcnt(27)
	v_cvt_pk_f16_f32 v4, v68, v69
	v_cvt_pk_f16_f32 v5, v70, v71
	ds_write_b64 v111, v[4:5] offset:15232
	global_load_dwordx4 v[68:71], v2, s[66:67] offset:2048 sc1 nt
	s_waitcnt lgkmcnt(0)
	s_barrier
	s_waitcnt vmcnt(27)
	v_cvt_pk_f16_f32 v4, v72, v73
	v_cvt_pk_f16_f32 v5, v74, v75
	ds_write_b64 v112, v[4:5]
	global_load_dwordx4 v[72:75], v2, s[52:53] offset:2560 sc1 nt
	s_waitcnt vmcnt(27)
	v_cvt_pk_f16_f32 v4, v76, v77
	v_cvt_pk_f16_f32 v5, v78, v79
	ds_write_b64 v112, v[4:5] offset:2176
	global_load_dwordx4 v[76:79], v2, s[54:55] offset:2560 sc1 nt
	s_waitcnt vmcnt(27)
	v_cvt_pk_f16_f32 v4, v80, v81
	v_cvt_pk_f16_f32 v5, v82, v83
	ds_write_b64 v112, v[4:5] offset:4352
	global_load_dwordx4 v[80:83], v2, s[56:57] offset:2560 sc1 nt
	s_waitcnt vmcnt(27)
	v_cvt_pk_f16_f32 v4, v84, v85
	v_cvt_pk_f16_f32 v5, v86, v87
	ds_write_b64 v112, v[4:5] offset:6528
	global_load_dwordx4 v[84:87], v2, s[58:59] offset:2560 sc1 nt
	s_waitcnt vmcnt(27)
	v_cvt_pk_f16_f32 v4, v88, v89
	v_cvt_pk_f16_f32 v5, v90, v91
	ds_write_b64 v112, v[4:5] offset:8704
	global_load_dwordx4 v[88:91], v2, s[60:61] offset:2560 sc1 nt
	s_waitcnt vmcnt(27)
	v_cvt_pk_f16_f32 v4, v92, v93
	v_cvt_pk_f16_f32 v5, v94, v95
	ds_write_b64 v112, v[4:5] offset:10880
	global_load_dwordx4 v[92:95], v2, s[62:63] offset:2560 sc1 nt
	s_waitcnt vmcnt(27)
	v_cvt_pk_f16_f32 v4, v96, v97
	v_cvt_pk_f16_f32 v5, v98, v99
	ds_write_b64 v112, v[4:5] offset:13056
	global_load_dwordx4 v[96:99], v2, s[64:65] offset:2560 sc1 nt
	s_waitcnt vmcnt(27)
	v_cvt_pk_f16_f32 v4, v100, v101
	v_cvt_pk_f16_f32 v5, v102, v103
	ds_write_b64 v112, v[4:5] offset:15232
	global_load_dwordx4 v[100:103], v2, s[66:67] offset:2560 sc1 nt
	s_waitcnt lgkmcnt(0)
	s_barrier
	s_waitcnt vmcnt(23)
	v_cvt_pk_f16_f32 v4, v8, v9
	v_cvt_pk_f16_f32 v5, v10, v11
	ds_write_b64 v110, v[4:5]
	global_load_dwordx4 v[8:11], v2, s[52:53] offset:3072 sc1 nt
	s_waitcnt vmcnt(23)
	v_cvt_pk_f16_f32 v4, v12, v13
	v_cvt_pk_f16_f32 v5, v14, v15
	ds_write_b64 v110, v[4:5] offset:2176
	global_load_dwordx4 v[12:15], v2, s[54:55] offset:3072 sc1 nt
	s_waitcnt vmcnt(23)
	v_cvt_pk_f16_f32 v4, v16, v17
	v_cvt_pk_f16_f32 v5, v18, v19
	ds_write_b64 v110, v[4:5] offset:4352
	global_load_dwordx4 v[16:19], v2, s[56:57] offset:3072 sc1 nt
	s_waitcnt vmcnt(23)
	v_cvt_pk_f16_f32 v4, v20, v21
	v_cvt_pk_f16_f32 v5, v22, v23
	ds_write_b64 v110, v[4:5] offset:6528
	global_load_dwordx4 v[20:23], v2, s[58:59] offset:3072 sc1 nt
	s_waitcnt vmcnt(23)
	v_cvt_pk_f16_f32 v4, v24, v25
	v_cvt_pk_f16_f32 v5, v26, v27
	ds_write_b64 v110, v[4:5] offset:8704
	global_load_dwordx4 v[24:27], v2, s[60:61] offset:3072 sc1 nt
	s_waitcnt vmcnt(23)
	v_cvt_pk_f16_f32 v4, v28, v29
	v_cvt_pk_f16_f32 v5, v30, v31
	ds_write_b64 v110, v[4:5] offset:10880
	global_load_dwordx4 v[28:31], v2, s[62:63] offset:3072 sc1 nt
	s_waitcnt vmcnt(23)
	v_cvt_pk_f16_f32 v4, v32, v33
	v_cvt_pk_f16_f32 v5, v34, v35
	ds_write_b64 v110, v[4:5] offset:13056
	global_load_dwordx4 v[32:35], v2, s[64:65] offset:3072 sc1 nt
	s_waitcnt vmcnt(23)
	v_cvt_pk_f16_f32 v4, v36, v37
	v_cvt_pk_f16_f32 v5, v38, v39
	ds_write_b64 v110, v[4:5] offset:15232
	global_load_dwordx4 v[36:39], v2, s[66:67] offset:3072 sc1 nt
	s_waitcnt lgkmcnt(0)
	s_barrier
	s_waitcnt vmcnt(23)
	v_cvt_pk_f16_f32 v4, v40, v41
	v_cvt_pk_f16_f32 v5, v42, v43
	ds_write_b64 v111, v[4:5]
	global_load_dwordx4 v[40:43], v2, s[52:53] offset:3584 sc1 nt
	s_waitcnt vmcnt(23)
	v_cvt_pk_f16_f32 v4, v44, v45
	v_cvt_pk_f16_f32 v5, v46, v47
	ds_write_b64 v111, v[4:5] offset:2176
	global_load_dwordx4 v[44:47], v2, s[54:55] offset:3584 sc1 nt
	s_waitcnt vmcnt(23)
	v_cvt_pk_f16_f32 v4, v48, v49
	v_cvt_pk_f16_f32 v5, v50, v51
	ds_write_b64 v111, v[4:5] offset:4352
	global_load_dwordx4 v[48:51], v2, s[56:57] offset:3584 sc1 nt
	s_waitcnt vmcnt(23)
	v_cvt_pk_f16_f32 v4, v52, v53
	v_cvt_pk_f16_f32 v5, v54, v55
	ds_write_b64 v111, v[4:5] offset:6528
	global_load_dwordx4 v[52:55], v2, s[58:59] offset:3584 sc1 nt
	s_waitcnt vmcnt(23)
	v_cvt_pk_f16_f32 v4, v56, v57
	v_cvt_pk_f16_f32 v5, v58, v59
	ds_write_b64 v111, v[4:5] offset:8704
	global_load_dwordx4 v[56:59], v2, s[60:61] offset:3584 sc1 nt
	s_waitcnt vmcnt(23)
	v_cvt_pk_f16_f32 v4, v60, v61
	v_cvt_pk_f16_f32 v5, v62, v63
	ds_write_b64 v111, v[4:5] offset:10880
	global_load_dwordx4 v[60:63], v2, s[62:63] offset:3584 sc1 nt
	s_waitcnt vmcnt(23)
	v_cvt_pk_f16_f32 v4, v64, v65
	v_cvt_pk_f16_f32 v5, v66, v67
	ds_write_b64 v111, v[4:5] offset:13056
	global_load_dwordx4 v[64:67], v2, s[64:65] offset:3584 sc1 nt
	s_waitcnt vmcnt(23)
	v_cvt_pk_f16_f32 v4, v68, v69
	v_cvt_pk_f16_f32 v5, v70, v71
	ds_write_b64 v111, v[4:5] offset:15232
	global_load_dwordx4 v[68:71], v2, s[66:67] offset:3584 sc1 nt
	s_waitcnt lgkmcnt(0)
	s_barrier
	s_waitcnt vmcnt(23)
	v_cvt_pk_f16_f32 v4, v72, v73
	v_cvt_pk_f16_f32 v5, v74, v75
	ds_write_b64 v112, v[4:5]
	v_add_u32_e32 v2, 0x1000, v2
	global_load_dwordx4 v[72:75], v2, s[52:53] sc1 nt
	s_waitcnt vmcnt(23)
	v_cvt_pk_f16_f32 v4, v76, v77
	v_cvt_pk_f16_f32 v5, v78, v79
	ds_write_b64 v112, v[4:5] offset:2176
	global_load_dwordx4 v[76:79], v2, s[54:55] sc1 nt
	s_waitcnt vmcnt(23)
	v_cvt_pk_f16_f32 v4, v80, v81
	v_cvt_pk_f16_f32 v5, v82, v83
	ds_write_b64 v112, v[4:5] offset:4352
	global_load_dwordx4 v[80:83], v2, s[56:57] sc1 nt
	s_waitcnt vmcnt(23)
	v_cvt_pk_f16_f32 v4, v84, v85
	v_cvt_pk_f16_f32 v5, v86, v87
	ds_write_b64 v112, v[4:5] offset:6528
	global_load_dwordx4 v[84:87], v2, s[58:59] sc1 nt
	s_waitcnt vmcnt(23)
	v_cvt_pk_f16_f32 v4, v88, v89
	v_cvt_pk_f16_f32 v5, v90, v91
	ds_write_b64 v112, v[4:5] offset:8704
	global_load_dwordx4 v[88:91], v2, s[60:61] sc1 nt
	s_waitcnt vmcnt(23)
	v_cvt_pk_f16_f32 v4, v92, v93
	v_cvt_pk_f16_f32 v5, v94, v95
	ds_write_b64 v112, v[4:5] offset:10880
	global_load_dwordx4 v[92:95], v2, s[62:63] sc1 nt
	s_waitcnt vmcnt(23)
	v_cvt_pk_f16_f32 v4, v96, v97
	v_cvt_pk_f16_f32 v5, v98, v99
	ds_write_b64 v112, v[4:5] offset:13056
	global_load_dwordx4 v[96:99], v2, s[64:65] sc1 nt
	s_waitcnt vmcnt(23)
	v_cvt_pk_f16_f32 v4, v100, v101
	v_cvt_pk_f16_f32 v5, v102, v103
	ds_write_b64 v112, v[4:5] offset:15232
	global_load_dwordx4 v[100:103], v2, s[66:67] sc1 nt
	s_waitcnt lgkmcnt(0)
	s_barrier
	s_waitcnt vmcnt(23)
	v_cvt_pk_f16_f32 v4, v8, v9
	v_cvt_pk_f16_f32 v5, v10, v11
	ds_write_b64 v110, v[4:5]
	global_load_dwordx4 v[8:11], v2, s[52:53] offset:512 sc1 nt
	s_waitcnt vmcnt(23)
	v_cvt_pk_f16_f32 v4, v12, v13
	v_cvt_pk_f16_f32 v5, v14, v15
	ds_write_b64 v110, v[4:5] offset:2176
	global_load_dwordx4 v[12:15], v2, s[54:55] offset:512 sc1 nt
	s_waitcnt vmcnt(23)
	v_cvt_pk_f16_f32 v4, v16, v17
	v_cvt_pk_f16_f32 v5, v18, v19
	ds_write_b64 v110, v[4:5] offset:4352
	global_load_dwordx4 v[16:19], v2, s[56:57] offset:512 sc1 nt
	s_waitcnt vmcnt(23)
	v_cvt_pk_f16_f32 v4, v20, v21
	v_cvt_pk_f16_f32 v5, v22, v23
	ds_write_b64 v110, v[4:5] offset:6528
	global_load_dwordx4 v[20:23], v2, s[58:59] offset:512 sc1 nt
	s_waitcnt vmcnt(23)
	v_cvt_pk_f16_f32 v4, v24, v25
	v_cvt_pk_f16_f32 v5, v26, v27
	ds_write_b64 v110, v[4:5] offset:8704
	global_load_dwordx4 v[24:27], v2, s[60:61] offset:512 sc1 nt
	s_waitcnt vmcnt(23)
	v_cvt_pk_f16_f32 v4, v28, v29
	v_cvt_pk_f16_f32 v5, v30, v31
	ds_write_b64 v110, v[4:5] offset:10880
	global_load_dwordx4 v[28:31], v2, s[62:63] offset:512 sc1 nt
	s_waitcnt vmcnt(23)
	v_cvt_pk_f16_f32 v4, v32, v33
	v_cvt_pk_f16_f32 v5, v34, v35
	ds_write_b64 v110, v[4:5] offset:13056
	global_load_dwordx4 v[32:35], v2, s[64:65] offset:512 sc1 nt
	s_waitcnt vmcnt(23)
	v_cvt_pk_f16_f32 v4, v36, v37
	v_cvt_pk_f16_f32 v5, v38, v39
	ds_write_b64 v110, v[4:5] offset:15232
	global_load_dwordx4 v[36:39], v2, s[66:67] offset:512 sc1 nt
	s_waitcnt lgkmcnt(0)
	s_barrier
	s_waitcnt vmcnt(23)
	v_cvt_pk_f16_f32 v4, v40, v41
	v_cvt_pk_f16_f32 v5, v42, v43
	ds_write_b64 v111, v[4:5]
	global_load_dwordx4 v[40:43], v2, s[52:53] offset:1024 sc1 nt
	s_waitcnt vmcnt(23)
	v_cvt_pk_f16_f32 v4, v44, v45
	v_cvt_pk_f16_f32 v5, v46, v47
	ds_write_b64 v111, v[4:5] offset:2176
	global_load_dwordx4 v[44:47], v2, s[54:55] offset:1024 sc1 nt
	s_waitcnt vmcnt(23)
	v_cvt_pk_f16_f32 v4, v48, v49
	v_cvt_pk_f16_f32 v5, v50, v51
	ds_write_b64 v111, v[4:5] offset:4352
	global_load_dwordx4 v[48:51], v2, s[56:57] offset:1024 sc1 nt
	s_waitcnt vmcnt(23)
	v_cvt_pk_f16_f32 v4, v52, v53
	v_cvt_pk_f16_f32 v5, v54, v55
	ds_write_b64 v111, v[4:5] offset:6528
	global_load_dwordx4 v[52:55], v2, s[58:59] offset:1024 sc1 nt
	s_waitcnt vmcnt(23)
	v_cvt_pk_f16_f32 v4, v56, v57
	v_cvt_pk_f16_f32 v5, v58, v59
	ds_write_b64 v111, v[4:5] offset:8704
	global_load_dwordx4 v[56:59], v2, s[60:61] offset:1024 sc1 nt
	s_waitcnt vmcnt(23)
	v_cvt_pk_f16_f32 v4, v60, v61
	v_cvt_pk_f16_f32 v5, v62, v63
	ds_write_b64 v111, v[4:5] offset:10880
	global_load_dwordx4 v[60:63], v2, s[62:63] offset:1024 sc1 nt
	s_waitcnt vmcnt(23)
	v_cvt_pk_f16_f32 v4, v64, v65
	v_cvt_pk_f16_f32 v5, v66, v67
	ds_write_b64 v111, v[4:5] offset:13056
	global_load_dwordx4 v[64:67], v2, s[64:65] offset:1024 sc1 nt
	s_waitcnt vmcnt(23)
	v_cvt_pk_f16_f32 v4, v68, v69
	v_cvt_pk_f16_f32 v5, v70, v71
	ds_write_b64 v111, v[4:5] offset:15232
	global_load_dwordx4 v[68:71], v2, s[66:67] offset:1024 sc1 nt
	s_waitcnt lgkmcnt(0)
	s_barrier
	s_waitcnt vmcnt(23)
	v_cvt_pk_f16_f32 v4, v72, v73
	v_cvt_pk_f16_f32 v5, v74, v75
	ds_write_b64 v112, v[4:5]
	global_load_dwordx4 v[72:75], v2, s[52:53] offset:1536 sc1 nt
	s_waitcnt vmcnt(23)
	v_cvt_pk_f16_f32 v4, v76, v77
	v_cvt_pk_f16_f32 v5, v78, v79
	ds_write_b64 v112, v[4:5] offset:2176
	global_load_dwordx4 v[76:79], v2, s[54:55] offset:1536 sc1 nt
	s_waitcnt vmcnt(23)
	v_cvt_pk_f16_f32 v4, v80, v81
	v_cvt_pk_f16_f32 v5, v82, v83
	ds_write_b64 v112, v[4:5] offset:4352
	global_load_dwordx4 v[80:83], v2, s[56:57] offset:1536 sc1 nt
	s_waitcnt vmcnt(23)
	v_cvt_pk_f16_f32 v4, v84, v85
	v_cvt_pk_f16_f32 v5, v86, v87
	ds_write_b64 v112, v[4:5] offset:6528
	global_load_dwordx4 v[84:87], v2, s[58:59] offset:1536 sc1 nt
	s_waitcnt vmcnt(23)
	v_cvt_pk_f16_f32 v4, v88, v89
	v_cvt_pk_f16_f32 v5, v90, v91
	ds_write_b64 v112, v[4:5] offset:8704
	global_load_dwordx4 v[88:91], v2, s[60:61] offset:1536 sc1 nt
	s_waitcnt vmcnt(23)
	v_cvt_pk_f16_f32 v4, v92, v93
	v_cvt_pk_f16_f32 v5, v94, v95
	ds_write_b64 v112, v[4:5] offset:10880
	global_load_dwordx4 v[92:95], v2, s[62:63] offset:1536 sc1 nt
	s_waitcnt vmcnt(23)
	v_cvt_pk_f16_f32 v4, v96, v97
	v_cvt_pk_f16_f32 v5, v98, v99
	ds_write_b64 v112, v[4:5] offset:13056
	global_load_dwordx4 v[96:99], v2, s[64:65] offset:1536 sc1 nt
	s_waitcnt vmcnt(23)
	v_cvt_pk_f16_f32 v4, v100, v101
	v_cvt_pk_f16_f32 v5, v102, v103
	ds_write_b64 v112, v[4:5] offset:15232
	global_load_dwordx4 v[100:103], v2, s[66:67] offset:1536 sc1 nt
	s_waitcnt lgkmcnt(0)
	s_barrier
	s_waitcnt vmcnt(23)
	v_cvt_pk_f16_f32 v4, v8, v9
	v_cvt_pk_f16_f32 v5, v10, v11
	ds_write_b64 v110, v[4:5]
	global_load_dwordx4 v[8:11], v2, s[52:53] offset:2048 sc1 nt
	s_waitcnt vmcnt(23)
	v_cvt_pk_f16_f32 v4, v12, v13
	v_cvt_pk_f16_f32 v5, v14, v15
	ds_write_b64 v110, v[4:5] offset:2176
	global_load_dwordx4 v[12:15], v2, s[54:55] offset:2048 sc1 nt
	s_waitcnt vmcnt(23)
	v_cvt_pk_f16_f32 v4, v16, v17
	v_cvt_pk_f16_f32 v5, v18, v19
	ds_write_b64 v110, v[4:5] offset:4352
	global_load_dwordx4 v[16:19], v2, s[56:57] offset:2048 sc1 nt
	s_waitcnt vmcnt(23)
	v_cvt_pk_f16_f32 v4, v20, v21
	v_cvt_pk_f16_f32 v5, v22, v23
	ds_write_b64 v110, v[4:5] offset:6528
	global_load_dwordx4 v[20:23], v2, s[58:59] offset:2048 sc1 nt
	s_waitcnt vmcnt(23)
	v_cvt_pk_f16_f32 v4, v24, v25
	v_cvt_pk_f16_f32 v5, v26, v27
	ds_write_b64 v110, v[4:5] offset:8704
	global_load_dwordx4 v[24:27], v2, s[60:61] offset:2048 sc1 nt
	s_waitcnt vmcnt(23)
	v_cvt_pk_f16_f32 v4, v28, v29
	v_cvt_pk_f16_f32 v5, v30, v31
	ds_write_b64 v110, v[4:5] offset:10880
	global_load_dwordx4 v[28:31], v2, s[62:63] offset:2048 sc1 nt
	s_waitcnt vmcnt(23)
	v_cvt_pk_f16_f32 v4, v32, v33
	v_cvt_pk_f16_f32 v5, v34, v35
	ds_write_b64 v110, v[4:5] offset:13056
	global_load_dwordx4 v[32:35], v2, s[64:65] offset:2048 sc1 nt
	s_waitcnt vmcnt(23)
	v_cvt_pk_f16_f32 v4, v36, v37
	v_cvt_pk_f16_f32 v5, v38, v39
	ds_write_b64 v110, v[4:5] offset:15232
	global_load_dwordx4 v[36:39], v2, s[66:67] offset:2048 sc1 nt
	s_waitcnt lgkmcnt(0)
	s_barrier
	s_waitcnt vmcnt(23)
	v_cvt_pk_f16_f32 v4, v40, v41
	v_cvt_pk_f16_f32 v5, v42, v43
	ds_write_b64 v111, v[4:5]
	global_load_dwordx4 v[40:43], v2, s[52:53] offset:2560 sc1 nt
	s_waitcnt vmcnt(23)
	v_cvt_pk_f16_f32 v4, v44, v45
	v_cvt_pk_f16_f32 v5, v46, v47
	ds_write_b64 v111, v[4:5] offset:2176
	global_load_dwordx4 v[44:47], v2, s[54:55] offset:2560 sc1 nt
	s_waitcnt vmcnt(23)
	v_cvt_pk_f16_f32 v4, v48, v49
	v_cvt_pk_f16_f32 v5, v50, v51
	ds_write_b64 v111, v[4:5] offset:4352
	global_load_dwordx4 v[48:51], v2, s[56:57] offset:2560 sc1 nt
	s_waitcnt vmcnt(23)
	v_cvt_pk_f16_f32 v4, v52, v53
	v_cvt_pk_f16_f32 v5, v54, v55
	ds_write_b64 v111, v[4:5] offset:6528
	global_load_dwordx4 v[52:55], v2, s[58:59] offset:2560 sc1 nt
	s_waitcnt vmcnt(23)
	v_cvt_pk_f16_f32 v4, v56, v57
	v_cvt_pk_f16_f32 v5, v58, v59
	ds_write_b64 v111, v[4:5] offset:8704
	global_load_dwordx4 v[56:59], v2, s[60:61] offset:2560 sc1 nt
	s_waitcnt vmcnt(23)
	v_cvt_pk_f16_f32 v4, v60, v61
	v_cvt_pk_f16_f32 v5, v62, v63
	ds_write_b64 v111, v[4:5] offset:10880
	global_load_dwordx4 v[60:63], v2, s[62:63] offset:2560 sc1 nt
	s_waitcnt vmcnt(23)
	v_cvt_pk_f16_f32 v4, v64, v65
	v_cvt_pk_f16_f32 v5, v66, v67
	ds_write_b64 v111, v[4:5] offset:13056
	global_load_dwordx4 v[64:67], v2, s[64:65] offset:2560 sc1 nt
	s_waitcnt vmcnt(23)
	v_cvt_pk_f16_f32 v4, v68, v69
	v_cvt_pk_f16_f32 v5, v70, v71
	ds_write_b64 v111, v[4:5] offset:15232
	global_load_dwordx4 v[68:71], v2, s[66:67] offset:2560 sc1 nt
	s_waitcnt lgkmcnt(0)
	s_barrier
	s_waitcnt vmcnt(23)
	v_cvt_pk_f16_f32 v4, v72, v73
	v_cvt_pk_f16_f32 v5, v74, v75
	ds_write_b64 v112, v[4:5]
	global_load_dwordx4 v[72:75], v2, s[52:53] offset:3072 sc1 nt
	s_waitcnt vmcnt(23)
	v_cvt_pk_f16_f32 v4, v76, v77
	v_cvt_pk_f16_f32 v5, v78, v79
	ds_write_b64 v112, v[4:5] offset:2176
	global_load_dwordx4 v[76:79], v2, s[54:55] offset:3072 sc1 nt
	s_waitcnt vmcnt(23)
	v_cvt_pk_f16_f32 v4, v80, v81
	v_cvt_pk_f16_f32 v5, v82, v83
	ds_write_b64 v112, v[4:5] offset:4352
	global_load_dwordx4 v[80:83], v2, s[56:57] offset:3072 sc1 nt
	s_waitcnt vmcnt(23)
	v_cvt_pk_f16_f32 v4, v84, v85
	v_cvt_pk_f16_f32 v5, v86, v87
	ds_write_b64 v112, v[4:5] offset:6528
	global_load_dwordx4 v[84:87], v2, s[58:59] offset:3072 sc1 nt
	s_waitcnt vmcnt(23)
	v_cvt_pk_f16_f32 v4, v88, v89
	v_cvt_pk_f16_f32 v5, v90, v91
	ds_write_b64 v112, v[4:5] offset:8704
	global_load_dwordx4 v[88:91], v2, s[60:61] offset:3072 sc1 nt
	s_waitcnt vmcnt(23)
	v_cvt_pk_f16_f32 v4, v92, v93
	v_cvt_pk_f16_f32 v5, v94, v95
	ds_write_b64 v112, v[4:5] offset:10880
	global_load_dwordx4 v[92:95], v2, s[62:63] offset:3072 sc1 nt
	s_waitcnt vmcnt(23)
	v_cvt_pk_f16_f32 v4, v96, v97
	v_cvt_pk_f16_f32 v5, v98, v99
	ds_write_b64 v112, v[4:5] offset:13056
	global_load_dwordx4 v[96:99], v2, s[64:65] offset:3072 sc1 nt
	s_waitcnt vmcnt(23)
	v_cvt_pk_f16_f32 v4, v100, v101
	v_cvt_pk_f16_f32 v5, v102, v103
	ds_write_b64 v112, v[4:5] offset:15232
	global_load_dwordx4 v[100:103], v2, s[66:67] offset:3072 sc1 nt
	s_waitcnt lgkmcnt(0)
	s_barrier
	s_waitcnt vmcnt(23)
	v_cvt_pk_f16_f32 v4, v8, v9
	v_cvt_pk_f16_f32 v5, v10, v11
	ds_write_b64 v110, v[4:5]
	global_load_dwordx4 v[8:11], v2, s[52:53] offset:3584 sc1 nt
	s_waitcnt vmcnt(23)
	v_cvt_pk_f16_f32 v4, v12, v13
	v_cvt_pk_f16_f32 v5, v14, v15
	ds_write_b64 v110, v[4:5] offset:2176
	global_load_dwordx4 v[12:15], v2, s[54:55] offset:3584 sc1 nt
	s_waitcnt vmcnt(23)
	v_cvt_pk_f16_f32 v4, v16, v17
	v_cvt_pk_f16_f32 v5, v18, v19
	ds_write_b64 v110, v[4:5] offset:4352
	global_load_dwordx4 v[16:19], v2, s[56:57] offset:3584 sc1 nt
	s_waitcnt vmcnt(23)
	v_cvt_pk_f16_f32 v4, v20, v21
	v_cvt_pk_f16_f32 v5, v22, v23
	ds_write_b64 v110, v[4:5] offset:6528
	global_load_dwordx4 v[20:23], v2, s[58:59] offset:3584 sc1 nt
	s_waitcnt vmcnt(23)
	v_cvt_pk_f16_f32 v4, v24, v25
	v_cvt_pk_f16_f32 v5, v26, v27
	ds_write_b64 v110, v[4:5] offset:8704
	global_load_dwordx4 v[24:27], v2, s[60:61] offset:3584 sc1 nt
	s_waitcnt vmcnt(23)
	v_cvt_pk_f16_f32 v4, v28, v29
	v_cvt_pk_f16_f32 v5, v30, v31
	ds_write_b64 v110, v[4:5] offset:10880
	global_load_dwordx4 v[28:31], v2, s[62:63] offset:3584 sc1 nt
	s_waitcnt vmcnt(23)
	v_cvt_pk_f16_f32 v4, v32, v33
	v_cvt_pk_f16_f32 v5, v34, v35
	ds_write_b64 v110, v[4:5] offset:13056
	global_load_dwordx4 v[32:35], v2, s[64:65] offset:3584 sc1 nt
	s_waitcnt vmcnt(23)
	v_cvt_pk_f16_f32 v4, v36, v37
	v_cvt_pk_f16_f32 v5, v38, v39
	ds_write_b64 v110, v[4:5] offset:15232
	global_load_dwordx4 v[36:39], v2, s[66:67] offset:3584 sc1 nt
	s_waitcnt lgkmcnt(0)
	s_barrier
	s_waitcnt vmcnt(23)
	v_cvt_pk_f16_f32 v4, v40, v41
	v_cvt_pk_f16_f32 v5, v42, v43
	ds_write_b64 v111, v[4:5]
	v_add_u32_e32 v2, 0x1000, v2
	global_load_dwordx4 v[40:43], v2, s[52:53] sc1 nt
	s_waitcnt vmcnt(23)
	v_cvt_pk_f16_f32 v4, v44, v45
	v_cvt_pk_f16_f32 v5, v46, v47
	ds_write_b64 v111, v[4:5] offset:2176
	global_load_dwordx4 v[44:47], v2, s[54:55] sc1 nt
	s_waitcnt vmcnt(23)
	v_cvt_pk_f16_f32 v4, v48, v49
	v_cvt_pk_f16_f32 v5, v50, v51
	ds_write_b64 v111, v[4:5] offset:4352
	global_load_dwordx4 v[48:51], v2, s[56:57] sc1 nt
	s_waitcnt vmcnt(23)
	v_cvt_pk_f16_f32 v4, v52, v53
	v_cvt_pk_f16_f32 v5, v54, v55
	ds_write_b64 v111, v[4:5] offset:6528
	global_load_dwordx4 v[52:55], v2, s[58:59] sc1 nt
	s_waitcnt vmcnt(23)
	v_cvt_pk_f16_f32 v4, v56, v57
	v_cvt_pk_f16_f32 v5, v58, v59
	ds_write_b64 v111, v[4:5] offset:8704
	global_load_dwordx4 v[56:59], v2, s[60:61] sc1 nt
	s_waitcnt vmcnt(23)
	v_cvt_pk_f16_f32 v4, v60, v61
	v_cvt_pk_f16_f32 v5, v62, v63
	ds_write_b64 v111, v[4:5] offset:10880
	global_load_dwordx4 v[60:63], v2, s[62:63] sc1 nt
	s_waitcnt vmcnt(23)
	v_cvt_pk_f16_f32 v4, v64, v65
	v_cvt_pk_f16_f32 v5, v66, v67
	ds_write_b64 v111, v[4:5] offset:13056
	global_load_dwordx4 v[64:67], v2, s[64:65] sc1 nt
	s_waitcnt vmcnt(23)
	v_cvt_pk_f16_f32 v4, v68, v69
	v_cvt_pk_f16_f32 v5, v70, v71
	ds_write_b64 v111, v[4:5] offset:15232
	global_load_dwordx4 v[68:71], v2, s[66:67] sc1 nt
	s_waitcnt lgkmcnt(0)
	s_barrier
	s_waitcnt vmcnt(23)
	v_cvt_pk_f16_f32 v4, v72, v73
	v_cvt_pk_f16_f32 v5, v74, v75
	ds_write_b64 v112, v[4:5]
	global_load_dwordx4 v[72:75], v2, s[52:53] offset:512 sc1 nt
	s_waitcnt vmcnt(23)
	v_cvt_pk_f16_f32 v4, v76, v77
	v_cvt_pk_f16_f32 v5, v78, v79
	ds_write_b64 v112, v[4:5] offset:2176
	global_load_dwordx4 v[76:79], v2, s[54:55] offset:512 sc1 nt
	s_waitcnt vmcnt(23)
	v_cvt_pk_f16_f32 v4, v80, v81
	v_cvt_pk_f16_f32 v5, v82, v83
	ds_write_b64 v112, v[4:5] offset:4352
	global_load_dwordx4 v[80:83], v2, s[56:57] offset:512 sc1 nt
	s_waitcnt vmcnt(23)
	v_cvt_pk_f16_f32 v4, v84, v85
	v_cvt_pk_f16_f32 v5, v86, v87
	ds_write_b64 v112, v[4:5] offset:6528
	global_load_dwordx4 v[84:87], v2, s[58:59] offset:512 sc1 nt
	s_waitcnt vmcnt(23)
	v_cvt_pk_f16_f32 v4, v88, v89
	v_cvt_pk_f16_f32 v5, v90, v91
	ds_write_b64 v112, v[4:5] offset:8704
	global_load_dwordx4 v[88:91], v2, s[60:61] offset:512 sc1 nt
	s_waitcnt vmcnt(23)
	v_cvt_pk_f16_f32 v4, v92, v93
	v_cvt_pk_f16_f32 v5, v94, v95
	ds_write_b64 v112, v[4:5] offset:10880
	global_load_dwordx4 v[92:95], v2, s[62:63] offset:512 sc1 nt
	s_waitcnt vmcnt(23)
	v_cvt_pk_f16_f32 v4, v96, v97
	v_cvt_pk_f16_f32 v5, v98, v99
	ds_write_b64 v112, v[4:5] offset:13056
	global_load_dwordx4 v[96:99], v2, s[64:65] offset:512 sc1 nt
	s_waitcnt vmcnt(23)
	v_cvt_pk_f16_f32 v4, v100, v101
	v_cvt_pk_f16_f32 v5, v102, v103
	ds_write_b64 v112, v[4:5] offset:15232
	global_load_dwordx4 v[100:103], v2, s[66:67] offset:512 sc1 nt
	s_waitcnt lgkmcnt(0)
	s_barrier
	s_waitcnt vmcnt(23)
	v_cvt_pk_f16_f32 v4, v8, v9
	v_cvt_pk_f16_f32 v5, v10, v11
	ds_write_b64 v110, v[4:5]
	global_load_dwordx4 v[8:11], v2, s[52:53] offset:1024 sc1 nt
	s_waitcnt vmcnt(23)
	v_cvt_pk_f16_f32 v4, v12, v13
	v_cvt_pk_f16_f32 v5, v14, v15
	ds_write_b64 v110, v[4:5] offset:2176
	global_load_dwordx4 v[12:15], v2, s[54:55] offset:1024 sc1 nt
	s_waitcnt vmcnt(23)
	v_cvt_pk_f16_f32 v4, v16, v17
	v_cvt_pk_f16_f32 v5, v18, v19
	ds_write_b64 v110, v[4:5] offset:4352
	global_load_dwordx4 v[16:19], v2, s[56:57] offset:1024 sc1 nt
	s_waitcnt vmcnt(23)
	v_cvt_pk_f16_f32 v4, v20, v21
	v_cvt_pk_f16_f32 v5, v22, v23
	ds_write_b64 v110, v[4:5] offset:6528
	global_load_dwordx4 v[20:23], v2, s[58:59] offset:1024 sc1 nt
	s_waitcnt vmcnt(23)
	v_cvt_pk_f16_f32 v4, v24, v25
	v_cvt_pk_f16_f32 v5, v26, v27
	ds_write_b64 v110, v[4:5] offset:8704
	global_load_dwordx4 v[24:27], v2, s[60:61] offset:1024 sc1 nt
	s_waitcnt vmcnt(23)
	v_cvt_pk_f16_f32 v4, v28, v29
	v_cvt_pk_f16_f32 v5, v30, v31
	ds_write_b64 v110, v[4:5] offset:10880
	global_load_dwordx4 v[28:31], v2, s[62:63] offset:1024 sc1 nt
	s_waitcnt vmcnt(23)
	v_cvt_pk_f16_f32 v4, v32, v33
	v_cvt_pk_f16_f32 v5, v34, v35
	ds_write_b64 v110, v[4:5] offset:13056
	global_load_dwordx4 v[32:35], v2, s[64:65] offset:1024 sc1 nt
	s_waitcnt vmcnt(23)
	v_cvt_pk_f16_f32 v4, v36, v37
	v_cvt_pk_f16_f32 v5, v38, v39
	ds_write_b64 v110, v[4:5] offset:15232
	global_load_dwordx4 v[36:39], v2, s[66:67] offset:1024 sc1 nt
	s_waitcnt lgkmcnt(0)
	s_barrier
	s_waitcnt vmcnt(23)
	v_cvt_pk_f16_f32 v4, v40, v41
	v_cvt_pk_f16_f32 v5, v42, v43
	ds_write_b64 v111, v[4:5]
	global_load_dwordx4 v[40:43], v2, s[52:53] offset:1536 sc1 nt
	s_waitcnt vmcnt(23)
	v_cvt_pk_f16_f32 v4, v44, v45
	v_cvt_pk_f16_f32 v5, v46, v47
	ds_write_b64 v111, v[4:5] offset:2176
	global_load_dwordx4 v[44:47], v2, s[54:55] offset:1536 sc1 nt
	s_waitcnt vmcnt(23)
	v_cvt_pk_f16_f32 v4, v48, v49
	v_cvt_pk_f16_f32 v5, v50, v51
	ds_write_b64 v111, v[4:5] offset:4352
	global_load_dwordx4 v[48:51], v2, s[56:57] offset:1536 sc1 nt
	s_waitcnt vmcnt(23)
	v_cvt_pk_f16_f32 v4, v52, v53
	v_cvt_pk_f16_f32 v5, v54, v55
	ds_write_b64 v111, v[4:5] offset:6528
	global_load_dwordx4 v[52:55], v2, s[58:59] offset:1536 sc1 nt
	s_waitcnt vmcnt(23)
	v_cvt_pk_f16_f32 v4, v56, v57
	v_cvt_pk_f16_f32 v5, v58, v59
	ds_write_b64 v111, v[4:5] offset:8704
	global_load_dwordx4 v[56:59], v2, s[60:61] offset:1536 sc1 nt
	s_waitcnt vmcnt(23)
	v_cvt_pk_f16_f32 v4, v60, v61
	v_cvt_pk_f16_f32 v5, v62, v63
	ds_write_b64 v111, v[4:5] offset:10880
	global_load_dwordx4 v[60:63], v2, s[62:63] offset:1536 sc1 nt
	s_waitcnt vmcnt(23)
	v_cvt_pk_f16_f32 v4, v64, v65
	v_cvt_pk_f16_f32 v5, v66, v67
	ds_write_b64 v111, v[4:5] offset:13056
	global_load_dwordx4 v[64:67], v2, s[64:65] offset:1536 sc1 nt
	s_waitcnt vmcnt(23)
	v_cvt_pk_f16_f32 v4, v68, v69
	v_cvt_pk_f16_f32 v5, v70, v71
	ds_write_b64 v111, v[4:5] offset:15232
	global_load_dwordx4 v[68:71], v2, s[66:67] offset:1536 sc1 nt
	s_waitcnt lgkmcnt(0)
	s_barrier
	s_waitcnt vmcnt(23)
	v_cvt_pk_f16_f32 v4, v72, v73
	v_cvt_pk_f16_f32 v5, v74, v75
	ds_write_b64 v112, v[4:5]
	global_load_dwordx4 v[72:75], v2, s[52:53] offset:2048 sc1 nt
	s_waitcnt vmcnt(23)
	v_cvt_pk_f16_f32 v4, v76, v77
	v_cvt_pk_f16_f32 v5, v78, v79
	ds_write_b64 v112, v[4:5] offset:2176
	global_load_dwordx4 v[76:79], v2, s[54:55] offset:2048 sc1 nt
	s_waitcnt vmcnt(23)
	v_cvt_pk_f16_f32 v4, v80, v81
	v_cvt_pk_f16_f32 v5, v82, v83
	ds_write_b64 v112, v[4:5] offset:4352
	global_load_dwordx4 v[80:83], v2, s[56:57] offset:2048 sc1 nt
	s_waitcnt vmcnt(23)
	v_cvt_pk_f16_f32 v4, v84, v85
	v_cvt_pk_f16_f32 v5, v86, v87
	ds_write_b64 v112, v[4:5] offset:6528
	global_load_dwordx4 v[84:87], v2, s[58:59] offset:2048 sc1 nt
	s_waitcnt vmcnt(23)
	v_cvt_pk_f16_f32 v4, v88, v89
	v_cvt_pk_f16_f32 v5, v90, v91
	ds_write_b64 v112, v[4:5] offset:8704
	global_load_dwordx4 v[88:91], v2, s[60:61] offset:2048 sc1 nt
	s_waitcnt vmcnt(23)
	v_cvt_pk_f16_f32 v4, v92, v93
	v_cvt_pk_f16_f32 v5, v94, v95
	ds_write_b64 v112, v[4:5] offset:10880
	global_load_dwordx4 v[92:95], v2, s[62:63] offset:2048 sc1 nt
	s_waitcnt vmcnt(23)
	v_cvt_pk_f16_f32 v4, v96, v97
	v_cvt_pk_f16_f32 v5, v98, v99
	ds_write_b64 v112, v[4:5] offset:13056
	global_load_dwordx4 v[96:99], v2, s[64:65] offset:2048 sc1 nt
	s_waitcnt vmcnt(23)
	v_cvt_pk_f16_f32 v4, v100, v101
	v_cvt_pk_f16_f32 v5, v102, v103
	ds_write_b64 v112, v[4:5] offset:15232
	global_load_dwordx4 v[100:103], v2, s[66:67] offset:2048 sc1 nt
	s_waitcnt lgkmcnt(0)
	s_barrier
	s_waitcnt vmcnt(23)
	v_cvt_pk_f16_f32 v4, v8, v9
	v_cvt_pk_f16_f32 v5, v10, v11
	ds_write_b64 v110, v[4:5]
	global_load_dwordx4 v[8:11], v2, s[52:53] offset:2560 sc1 nt
	s_waitcnt vmcnt(23)
	v_cvt_pk_f16_f32 v4, v12, v13
	v_cvt_pk_f16_f32 v5, v14, v15
	ds_write_b64 v110, v[4:5] offset:2176
	global_load_dwordx4 v[12:15], v2, s[54:55] offset:2560 sc1 nt
	s_waitcnt vmcnt(23)
	v_cvt_pk_f16_f32 v4, v16, v17
	v_cvt_pk_f16_f32 v5, v18, v19
	ds_write_b64 v110, v[4:5] offset:4352
	global_load_dwordx4 v[16:19], v2, s[56:57] offset:2560 sc1 nt
	s_waitcnt vmcnt(23)
	v_cvt_pk_f16_f32 v4, v20, v21
	v_cvt_pk_f16_f32 v5, v22, v23
	ds_write_b64 v110, v[4:5] offset:6528
	global_load_dwordx4 v[20:23], v2, s[58:59] offset:2560 sc1 nt
	s_waitcnt vmcnt(23)
	v_cvt_pk_f16_f32 v4, v24, v25
	v_cvt_pk_f16_f32 v5, v26, v27
	ds_write_b64 v110, v[4:5] offset:8704
	global_load_dwordx4 v[24:27], v2, s[60:61] offset:2560 sc1 nt
	s_waitcnt vmcnt(23)
	v_cvt_pk_f16_f32 v4, v28, v29
	v_cvt_pk_f16_f32 v5, v30, v31
	ds_write_b64 v110, v[4:5] offset:10880
	global_load_dwordx4 v[28:31], v2, s[62:63] offset:2560 sc1 nt
	s_waitcnt vmcnt(23)
	v_cvt_pk_f16_f32 v4, v32, v33
	v_cvt_pk_f16_f32 v5, v34, v35
	ds_write_b64 v110, v[4:5] offset:13056
	global_load_dwordx4 v[32:35], v2, s[64:65] offset:2560 sc1 nt
	s_waitcnt vmcnt(23)
	v_cvt_pk_f16_f32 v4, v36, v37
	v_cvt_pk_f16_f32 v5, v38, v39
	ds_write_b64 v110, v[4:5] offset:15232
	global_load_dwordx4 v[36:39], v2, s[66:67] offset:2560 sc1 nt
	s_waitcnt lgkmcnt(0)
	s_barrier
	s_waitcnt vmcnt(23)
	v_cvt_pk_f16_f32 v4, v40, v41
	v_cvt_pk_f16_f32 v5, v42, v43
	ds_write_b64 v111, v[4:5]
	global_load_dwordx4 v[40:43], v2, s[52:53] offset:3072 sc1 nt
	s_waitcnt vmcnt(23)
	v_cvt_pk_f16_f32 v4, v44, v45
	v_cvt_pk_f16_f32 v5, v46, v47
	ds_write_b64 v111, v[4:5] offset:2176
	global_load_dwordx4 v[44:47], v2, s[54:55] offset:3072 sc1 nt
	s_waitcnt vmcnt(23)
	v_cvt_pk_f16_f32 v4, v48, v49
	v_cvt_pk_f16_f32 v5, v50, v51
	ds_write_b64 v111, v[4:5] offset:4352
	global_load_dwordx4 v[48:51], v2, s[56:57] offset:3072 sc1 nt
	s_waitcnt vmcnt(23)
	v_cvt_pk_f16_f32 v4, v52, v53
	v_cvt_pk_f16_f32 v5, v54, v55
	ds_write_b64 v111, v[4:5] offset:6528
	global_load_dwordx4 v[52:55], v2, s[58:59] offset:3072 sc1 nt
	s_waitcnt vmcnt(23)
	v_cvt_pk_f16_f32 v4, v56, v57
	v_cvt_pk_f16_f32 v5, v58, v59
	ds_write_b64 v111, v[4:5] offset:8704
	global_load_dwordx4 v[56:59], v2, s[60:61] offset:3072 sc1 nt
	s_waitcnt vmcnt(23)
	v_cvt_pk_f16_f32 v4, v60, v61
	v_cvt_pk_f16_f32 v5, v62, v63
	ds_write_b64 v111, v[4:5] offset:10880
	global_load_dwordx4 v[60:63], v2, s[62:63] offset:3072 sc1 nt
	s_waitcnt vmcnt(23)
	v_cvt_pk_f16_f32 v4, v64, v65
	v_cvt_pk_f16_f32 v5, v66, v67
	ds_write_b64 v111, v[4:5] offset:13056
	global_load_dwordx4 v[64:67], v2, s[64:65] offset:3072 sc1 nt
	s_waitcnt vmcnt(23)
	v_cvt_pk_f16_f32 v4, v68, v69
	v_cvt_pk_f16_f32 v5, v70, v71
	ds_write_b64 v111, v[4:5] offset:15232
	global_load_dwordx4 v[68:71], v2, s[66:67] offset:3072 sc1 nt
	s_waitcnt lgkmcnt(0)
	s_barrier
	s_waitcnt vmcnt(23)
	v_cvt_pk_f16_f32 v4, v72, v73
	v_cvt_pk_f16_f32 v5, v74, v75
	ds_write_b64 v112, v[4:5]
	v_mov_b32_e32 v72, 0
	v_mov_b32_e32 v73, 0
	v_mov_b32_e32 v74, 0
	v_mov_b32_e32 v75, 0
	s_mov_b64 s[70:71], exec
	s_mov_b64 exec, s[68:69]
	global_load_dwordx4 v[72:75], v2, s[52:53] offset:3584 sc1 nt
	s_mov_b64 exec, s[70:71]
	s_waitcnt vmcnt(23)
	v_cvt_pk_f16_f32 v4, v76, v77
	v_cvt_pk_f16_f32 v5, v78, v79
	ds_write_b64 v112, v[4:5] offset:2176
	v_mov_b32_e32 v76, 0
	v_mov_b32_e32 v77, 0
	v_mov_b32_e32 v78, 0
	v_mov_b32_e32 v79, 0
	s_mov_b64 s[70:71], exec
	s_mov_b64 exec, s[68:69]
	global_load_dwordx4 v[76:79], v2, s[54:55] offset:3584 sc1 nt
	s_mov_b64 exec, s[70:71]
	s_waitcnt vmcnt(23)
	v_cvt_pk_f16_f32 v4, v80, v81
	v_cvt_pk_f16_f32 v5, v82, v83
	ds_write_b64 v112, v[4:5] offset:4352
	v_mov_b32_e32 v80, 0
	v_mov_b32_e32 v81, 0
	v_mov_b32_e32 v82, 0
	v_mov_b32_e32 v83, 0
	s_mov_b64 s[70:71], exec
	s_mov_b64 exec, s[68:69]
	global_load_dwordx4 v[80:83], v2, s[56:57] offset:3584 sc1 nt
	s_mov_b64 exec, s[70:71]
	s_waitcnt vmcnt(23)
	v_cvt_pk_f16_f32 v4, v84, v85
	v_cvt_pk_f16_f32 v5, v86, v87
	ds_write_b64 v112, v[4:5] offset:6528
	v_mov_b32_e32 v84, 0
	v_mov_b32_e32 v85, 0
	v_mov_b32_e32 v86, 0
	v_mov_b32_e32 v87, 0
	s_mov_b64 s[70:71], exec
	s_mov_b64 exec, s[68:69]
	global_load_dwordx4 v[84:87], v2, s[58:59] offset:3584 sc1 nt
	s_mov_b64 exec, s[70:71]
	s_waitcnt vmcnt(23)
	v_cvt_pk_f16_f32 v4, v88, v89
	v_cvt_pk_f16_f32 v5, v90, v91
	ds_write_b64 v112, v[4:5] offset:8704
	v_mov_b32_e32 v88, 0
	v_mov_b32_e32 v89, 0
	v_mov_b32_e32 v90, 0
	v_mov_b32_e32 v91, 0
	s_mov_b64 s[70:71], exec
	s_mov_b64 exec, s[68:69]
	global_load_dwordx4 v[88:91], v2, s[60:61] offset:3584 sc1 nt
	s_mov_b64 exec, s[70:71]
	s_waitcnt vmcnt(23)
	v_cvt_pk_f16_f32 v4, v92, v93
	v_cvt_pk_f16_f32 v5, v94, v95
	ds_write_b64 v112, v[4:5] offset:10880
	v_mov_b32_e32 v92, 0
	v_mov_b32_e32 v93, 0
	v_mov_b32_e32 v94, 0
	v_mov_b32_e32 v95, 0
	s_mov_b64 s[70:71], exec
	s_mov_b64 exec, s[68:69]
	global_load_dwordx4 v[92:95], v2, s[62:63] offset:3584 sc1 nt
	s_mov_b64 exec, s[70:71]
	s_waitcnt vmcnt(23)
	v_cvt_pk_f16_f32 v4, v96, v97
	v_cvt_pk_f16_f32 v5, v98, v99
	ds_write_b64 v112, v[4:5] offset:13056
	v_mov_b32_e32 v96, 0
	v_mov_b32_e32 v97, 0
	v_mov_b32_e32 v98, 0
	v_mov_b32_e32 v99, 0
	s_mov_b64 s[70:71], exec
	s_mov_b64 exec, s[68:69]
	global_load_dwordx4 v[96:99], v2, s[64:65] offset:3584 sc1 nt
	s_mov_b64 exec, s[70:71]
	s_waitcnt vmcnt(23)
	v_cvt_pk_f16_f32 v4, v100, v101
	v_cvt_pk_f16_f32 v5, v102, v103
	ds_write_b64 v112, v[4:5] offset:15232
	v_mov_b32_e32 v100, 0
	v_mov_b32_e32 v101, 0
	v_mov_b32_e32 v102, 0
	v_mov_b32_e32 v103, 0
	s_mov_b64 s[70:71], exec
	s_mov_b64 exec, s[68:69]
	global_load_dwordx4 v[100:103], v2, s[66:67] offset:3584 sc1 nt
	s_mov_b64 exec, s[70:71]
	s_waitcnt lgkmcnt(0)
	s_barrier
	s_waitcnt vmcnt(23)
	v_cvt_pk_f16_f32 v4, v8, v9
	v_cvt_pk_f16_f32 v5, v10, v11
	ds_write_b64 v110, v[4:5]
	s_waitcnt vmcnt(22)
	v_cvt_pk_f16_f32 v4, v12, v13
	v_cvt_pk_f16_f32 v5, v14, v15
	ds_write_b64 v110, v[4:5] offset:2176
	s_waitcnt vmcnt(21)
	v_cvt_pk_f16_f32 v4, v16, v17
	v_cvt_pk_f16_f32 v5, v18, v19
	ds_write_b64 v110, v[4:5] offset:4352
	s_waitcnt vmcnt(20)
	v_cvt_pk_f16_f32 v4, v20, v21
	v_cvt_pk_f16_f32 v5, v22, v23
	ds_write_b64 v110, v[4:5] offset:6528
	s_waitcnt vmcnt(19)
	v_cvt_pk_f16_f32 v4, v24, v25
	v_cvt_pk_f16_f32 v5, v26, v27
	ds_write_b64 v110, v[4:5] offset:8704
	s_waitcnt vmcnt(18)
	v_cvt_pk_f16_f32 v4, v28, v29
	v_cvt_pk_f16_f32 v5, v30, v31
	ds_write_b64 v110, v[4:5] offset:10880
	s_waitcnt vmcnt(17)
	v_cvt_pk_f16_f32 v4, v32, v33
	v_cvt_pk_f16_f32 v5, v34, v35
	ds_write_b64 v110, v[4:5] offset:13056
	s_waitcnt vmcnt(16)
	v_cvt_pk_f16_f32 v4, v36, v37
	v_cvt_pk_f16_f32 v5, v38, v39
	ds_write_b64 v110, v[4:5] offset:15232
	s_waitcnt lgkmcnt(0)
	s_barrier
	s_waitcnt vmcnt(15)
	v_cvt_pk_f16_f32 v4, v40, v41
	v_cvt_pk_f16_f32 v5, v42, v43
	ds_write_b64 v111, v[4:5]
	s_waitcnt vmcnt(14)
	v_cvt_pk_f16_f32 v4, v44, v45
	v_cvt_pk_f16_f32 v5, v46, v47
	ds_write_b64 v111, v[4:5] offset:2176
	s_waitcnt vmcnt(13)
	v_cvt_pk_f16_f32 v4, v48, v49
	v_cvt_pk_f16_f32 v5, v50, v51
	ds_write_b64 v111, v[4:5] offset:4352
	s_waitcnt vmcnt(12)
	v_cvt_pk_f16_f32 v4, v52, v53
	v_cvt_pk_f16_f32 v5, v54, v55
	ds_write_b64 v111, v[4:5] offset:6528
	s_waitcnt vmcnt(11)
	v_cvt_pk_f16_f32 v4, v56, v57
	v_cvt_pk_f16_f32 v5, v58, v59
	ds_write_b64 v111, v[4:5] offset:8704
	s_waitcnt vmcnt(10)
	v_cvt_pk_f16_f32 v4, v60, v61
	v_cvt_pk_f16_f32 v5, v62, v63
	ds_write_b64 v111, v[4:5] offset:10880
	s_waitcnt vmcnt(9)
	v_cvt_pk_f16_f32 v4, v64, v65
	v_cvt_pk_f16_f32 v5, v66, v67
	ds_write_b64 v111, v[4:5] offset:13056
	s_waitcnt vmcnt(8)
	v_cvt_pk_f16_f32 v4, v68, v69
	v_cvt_pk_f16_f32 v5, v70, v71
	ds_write_b64 v111, v[4:5] offset:15232
	s_waitcnt lgkmcnt(0)
	s_barrier
	s_waitcnt vmcnt(7)
	v_cvt_pk_f16_f32 v4, v72, v73
	v_cvt_pk_f16_f32 v5, v74, v75
	s_mov_b64 s[70:71], exec
	s_mov_b64 exec, s[78:79]
	ds_write_b64 v112, v[4:5]
	s_mov_b64 exec, s[70:71]
	s_waitcnt vmcnt(6)
	v_cvt_pk_f16_f32 v4, v76, v77
	v_cvt_pk_f16_f32 v5, v78, v79
	s_mov_b64 s[70:71], exec
	s_mov_b64 exec, s[78:79]
	ds_write_b64 v112, v[4:5] offset:2176
	s_mov_b64 exec, s[70:71]
	s_waitcnt vmcnt(5)
	v_cvt_pk_f16_f32 v4, v80, v81
	v_cvt_pk_f16_f32 v5, v82, v83
	s_mov_b64 s[70:71], exec
	s_mov_b64 exec, s[78:79]
	ds_write_b64 v112, v[4:5] offset:4352
	s_mov_b64 exec, s[70:71]
	s_waitcnt vmcnt(4)
	v_cvt_pk_f16_f32 v4, v84, v85
	v_cvt_pk_f16_f32 v5, v86, v87
	s_mov_b64 s[70:71], exec
	s_mov_b64 exec, s[78:79]
	ds_write_b64 v112, v[4:5] offset:6528
	s_mov_b64 exec, s[70:71]
	s_waitcnt vmcnt(3)
	v_cvt_pk_f16_f32 v4, v88, v89
	v_cvt_pk_f16_f32 v5, v90, v91
	s_mov_b64 s[70:71], exec
	s_mov_b64 exec, s[78:79]
	ds_write_b64 v112, v[4:5] offset:8704
	s_mov_b64 exec, s[70:71]
	s_waitcnt vmcnt(2)
	v_cvt_pk_f16_f32 v4, v92, v93
	v_cvt_pk_f16_f32 v5, v94, v95
	s_mov_b64 s[70:71], exec
	s_mov_b64 exec, s[78:79]
	ds_write_b64 v112, v[4:5] offset:10880
	s_mov_b64 exec, s[70:71]
	s_waitcnt vmcnt(1)
	v_cvt_pk_f16_f32 v4, v96, v97
	v_cvt_pk_f16_f32 v5, v98, v99
	s_mov_b64 s[70:71], exec
	s_mov_b64 exec, s[78:79]
	ds_write_b64 v112, v[4:5] offset:13056
	s_mov_b64 exec, s[70:71]
	s_waitcnt vmcnt(0)
	v_cvt_pk_f16_f32 v4, v100, v101
	v_cvt_pk_f16_f32 v5, v102, v103
	s_mov_b64 s[70:71], exec
	s_mov_b64 exec, s[78:79]
	ds_write_b64 v112, v[4:5] offset:15232
	s_mov_b64 exec, s[70:71]
	s_waitcnt lgkmcnt(0)
	s_barrier
	s_barrier
	s_barrier
	s_endpgm
